# speedup vs baseline: 1.0057x; 1.0057x over previous
_Z9gemm_gldsILi256ELi192ELi4ELi2ELi2ELi4ELi8ELi0ELi4096ELi3072ELi1024EEvPKDF16_S1_PfPKfS4_PKiPDF16_S7_S7_:
	s_ashr_i32 s3, s2, 3
	s_lshr_b32 s9, s3, 30
	s_add_i32 s9, s3, s9
	s_lshl_b32 s8, s2, 1
	s_ashr_i32 s10, s9, 2
	s_and_b32 s9, s9, 0xfffffc
	s_lshl_b32 s2, s2, 3
	s_load_dwordx4 s[4:7], s[0:1], 0x0
	s_and_b32 s8, s8, 12
	s_sub_i32 s3, s3, s9
	s_and_b32 s20, s2, 8
	s_add_i32 s8, s8, s3
	s_add_i32 s20, s20, s10
	s_lshl_b32 s16, s8, 8
	s_mul_i32 s2, s20, 0xc0
	v_lshlrev_b32_e32 v139, 4, v0
	v_and_b32_e32 v1, 32, v0
	s_ashr_i32 s17, s16, 31
	s_ashr_i32 s3, s2, 31
	v_lshrrev_b32_e32 v2, 3, v0
	v_bfe_u32 v46, v0, 2, 4
	v_bitop3_b32 v1, v139, v1, 48 bitop3:0x6c
	s_lshl_b64 s[8:9], s[16:17], 11
	s_lshl_b64 s[10:11], s[2:3], 11
	v_and_or_b32 v2, v2, 48, v46
	v_and_or_b32 v47, v0, 64, v1
	s_waitcnt lgkmcnt(0)
	s_add_u32 s2, s4, s8
	s_addc_u32 s3, s5, s9
	v_lshl_or_b32 v2, v2, 11, v47
	v_lshrrev_b32_e32 v216, 3, v0
	v_and_b32_e32 v217, 7, v216
	v_and_b32_e32 v218, 7, v0
	v_xor_b32_e32 v217, v218, v217
	v_lshlrev_b32_e32 v217, 4, v217
	v_lshl_or_b32 v216, v216, 11, v217
	v_mov_b32_e32 v218, v216
	v_mov_b32_e32 v219, 0
	v_add_u32_e32 v194, 0x100, v2
	v_add_u32_e32 v195, 0x100, v218
	v_mov_b32_e32 v3, 0
	v_readfirstlane_b32 s4, v139
	v_or_b32_e32 v1, 0x2000, v139
	s_add_u32 s18, s6, s10
	v_lshl_add_u64 v[4:5], s[2:3], 0, v[2:3]
	s_mov_b32 m0, s4
	s_mov_b64 s[4:5], 0x20000
	v_readfirstlane_b32 s6, v1
	v_or_b32_e32 v1, 0x4000, v139
	s_addc_u32 s19, s7, s11
	v_readfirstlane_b32 s45, v139
	s_mov_b64 s[24:25], s[2:3]
	s_add_u32 s26, s2, 0x20000
	s_addc_u32 s27, s3, 0
	s_add_u32 s28, s2, 0x40000
	s_addc_u32 s29, s3, 0
	s_add_u32 s30, s2, 0x60000
	s_addc_u32 s31, s3, 0
	s_mov_b64 s[32:33], s[18:19]
	s_add_u32 s34, s18, 0x20000
	s_addc_u32 s35, s19, 0
	s_add_u32 s36, s18, 0x40000
	s_addc_u32 s37, s19, 0
	global_load_lds_dwordx4 v2, s[2:3]
	v_lshl_add_u64 v[8:9], v[4:5], 0, s[4:5]
	s_mov_b32 m0, s6
	s_mov_b64 s[6:7], 0x40000
	v_readfirstlane_b32 s8, v1
	global_load_lds_dwordx4 v[8:9], off
	v_lshl_add_u64 v[8:9], v[4:5], 0, s[6:7]
	s_mov_b32 m0, s8
	s_mov_b64 s[8:9], 0x60000
	v_or_b32_e32 v1, 0x6000, v139
	global_load_lds_dwordx4 v[8:9], off
	v_lshl_add_u64 v[8:9], v[4:5], 0, s[8:9]
	v_readfirstlane_b32 s8, v1
	v_or_b32_e32 v1, 0x8000, v139
	v_lshl_add_u64 v[6:7], s[18:19], 0, v[218:219]
	s_mov_b32 m0, s8
	v_readfirstlane_b32 s8, v1
	v_or_b32_e32 v1, 0xa000, v139
	global_load_lds_dwordx4 v[8:9], off
	s_mov_b32 m0, s8
	v_lshl_add_u64 v[8:9], v[6:7], 0, s[4:5]
	v_readfirstlane_b32 s4, v1
	v_or_b32_e32 v1, 0xc000, v139
	global_load_lds_dwordx4 v218, s[18:19]
	s_mov_b32 m0, s4
	v_readfirstlane_b32 s4, v1
	v_or_b32_e32 v1, 0xe000, v139
	global_load_lds_dwordx4 v[8:9], off
	v_lshl_add_u64 v[8:9], v[6:7], 0, s[6:7]
	s_mov_b32 m0, s4
	s_mov_b64 s[4:5], 0x80
	v_readfirstlane_b32 s6, v1
	v_or_b32_e32 v1, 0x10000, v139
	global_load_lds_dwordx4 v[8:9], off
	v_lshl_add_u64 v[8:9], v[4:5], 0, s[4:5]
	s_mov_b32 m0, s6
	s_mov_b64 s[6:7], 0x20080
	v_readfirstlane_b32 s8, v1
	v_or_b32_e32 v1, 0x12000, v139
	global_load_lds_dwordx4 v[8:9], off
	v_lshl_add_u64 v[8:9], v[4:5], 0, s[6:7]
	s_mov_b32 m0, s8
	v_readfirstlane_b32 s10, v1
	global_load_lds_dwordx4 v[8:9], off
	s_mov_b64 s[8:9], 0x40080
	s_mov_b32 m0, s10
	s_mov_b64 s[10:11], 0x60080
	v_or_b32_e32 v1, 0x14000, v139
	v_lshl_add_u64 v[8:9], v[4:5], 0, s[8:9]
	v_lshl_add_u64 v[4:5], v[4:5], 0, s[10:11]
	v_readfirstlane_b32 s10, v1
	global_load_lds_dwordx4 v[8:9], off
	s_mov_b32 m0, s10
	v_or_b32_e32 v1, 0x16000, v139
	global_load_lds_dwordx4 v[4:5], off
	v_lshl_add_u64 v[4:5], v[6:7], 0, s[4:5]
	v_readfirstlane_b32 s4, v1
	v_or_b32_e32 v1, 0x18000, v139
	s_mov_b32 m0, s4
	v_readfirstlane_b32 s4, v1
	v_or_b32_e32 v1, 0x1a000, v139
	global_load_lds_dwordx4 v[4:5], off
	v_lshl_add_u64 v[4:5], v[6:7], 0, s[6:7]
	s_mov_b32 m0, s4
	v_readfirstlane_b32 s4, v1
	global_load_lds_dwordx4 v[4:5], off
	v_lshl_add_u64 v[4:5], v[6:7], 0, s[8:9]
	s_mov_b32 m0, s4
	v_lshrrev_b32_e32 v2, 7, v0
	global_load_lds_dwordx4 v[4:5], off
	s_load_dwordx4 s[12:15], s[0:1], 0x38
	s_load_dwordx8 s[4:11], s[0:1], 0x18
	v_lshlrev_b32_e32 v4, 6, v0
	v_and_b32_e32 v138, 48, v0
	v_and_b32_e32 v4, 0x3c0, v4
	v_lshlrev_b32_e32 v6, 2, v0
	v_bfe_u32 v144, v0, 6, 1
	v_or_b32_e32 v14, v4, v138
	v_lshlrev_b32_e32 v5, 13, v2
	v_and_b32_e32 v15, 32, v6
	v_and_b32_e32 v1, 15, v0
	v_and_b32_e32 v216, 15, v0
	v_bfe_u32 v217, v0, 4, 2
	v_and_b32_e32 v6, 7, v216
	v_xor_b32_e32 v217, v217, v6
	v_lshlrev_b32_e32 v217, 4, v217
	v_lshl_or_b32 v216, v216, 7, v217
	v_mov_b32_e32 v151, v216
	v_bitop3_b32 v146, v5, v14, v15 bitop3:0xf6
	v_mul_u32_u24_e32 v152, 0x3000, v144
	v_lshl_or_b32 v145, v2, 6, s16
	v_or_b32_e32 v4, v145, v1
	v_ashrrev_i32_e32 v5, 31, v4
	s_waitcnt lgkmcnt(0)
	v_lshl_add_u64 v[4:5], v[4:5], 2, s[8:9]
	global_load_dword v150, v[4:5], off
	global_load_dword v149, v[4:5], off offset:64
	global_load_dword v148, v[4:5], off offset:128
	global_load_dword v147, v[4:5], off offset:192
	v_or_b32_e32 v153, v152, v216
	v_xor_b32_e32 v215, 64, v153
	v_mov_b32_e32 v48, v3
	v_mov_b32_e32 v49, v3
	v_mov_b32_e32 v50, v3
	v_mov_b32_e32 v51, v3
	v_mov_b32_e32 v52, v3
	v_mov_b32_e32 v53, v3
	v_mov_b32_e32 v54, v3
	v_mov_b32_e32 v55, v3
	v_mov_b32_e32 v56, v3
	v_mov_b32_e32 v57, v3
	v_mov_b32_e32 v58, v3
	v_mov_b32_e32 v59, v3
	v_mov_b32_e32 v60, v3
	v_mov_b32_e32 v61, v3
	v_mov_b32_e32 v62, v3
	v_mov_b32_e32 v63, v3
	v_mov_b32_e32 v64, v3
	v_mov_b32_e32 v65, v3
	v_mov_b32_e32 v66, v3
	v_mov_b32_e32 v67, v3
	v_mov_b32_e32 v68, v3
	v_mov_b32_e32 v69, v3
	v_mov_b32_e32 v70, v3
	v_mov_b32_e32 v71, v3
	v_mov_b32_e32 v72, v3
	v_mov_b32_e32 v73, v3
	v_mov_b32_e32 v74, v3
	v_mov_b32_e32 v75, v3
	v_mov_b32_e32 v76, v3
	v_mov_b32_e32 v77, v3
	v_mov_b32_e32 v86, v3
	v_mov_b32_e32 v87, v3
	v_mov_b32_e32 v88, v3
	v_mov_b32_e32 v89, v3
	v_mov_b32_e32 v98, v3
	v_mov_b32_e32 v99, v3
	v_mov_b32_e32 v100, v3
	v_mov_b32_e32 v101, v3
	v_mov_b32_e32 v130, v3
	v_mov_b32_e32 v131, v3
	v_mov_b32_e32 v132, v3
	v_mov_b32_e32 v133, v3
	v_mov_b32_e32 v78, v3
	v_mov_b32_e32 v79, v3
	v_mov_b32_e32 v80, v3
	v_mov_b32_e32 v81, v3
	v_mov_b32_e32 v82, v3
	v_mov_b32_e32 v83, v3
	v_mov_b32_e32 v84, v3
	v_mov_b32_e32 v85, v3
	v_mov_b32_e32 v90, v3
	v_mov_b32_e32 v91, v3
	v_mov_b32_e32 v92, v3
	v_mov_b32_e32 v93, v3
	v_mov_b32_e32 v94, v3
	v_mov_b32_e32 v95, v3
	v_mov_b32_e32 v96, v3
	v_mov_b32_e32 v97, v3
	v_mov_b32_e32 v102, v3
	v_mov_b32_e32 v103, v3
	v_mov_b32_e32 v104, v3
	v_mov_b32_e32 v105, v3
	v_mov_b32_e32 v106, v3
	v_mov_b32_e32 v107, v3
	v_mov_b32_e32 v108, v3
	v_mov_b32_e32 v109, v3
	v_mov_b32_e32 v110, v3
	v_mov_b32_e32 v111, v3
	v_mov_b32_e32 v112, v3
	v_mov_b32_e32 v113, v3
	v_mov_b32_e32 v114, v3
	v_mov_b32_e32 v115, v3
	v_mov_b32_e32 v116, v3
	v_mov_b32_e32 v117, v3
	v_mov_b32_e32 v118, v3
	v_mov_b32_e32 v119, v3
	v_mov_b32_e32 v120, v3
	v_mov_b32_e32 v121, v3
	v_mov_b32_e32 v122, v3
	v_mov_b32_e32 v123, v3
	v_mov_b32_e32 v124, v3
	v_mov_b32_e32 v125, v3
	v_mov_b32_e32 v134, v3
	v_mov_b32_e32 v135, v3
	v_mov_b32_e32 v136, v3
	v_mov_b32_e32 v137, v3
	v_mov_b32_e32 v126, v3
	v_mov_b32_e32 v127, v3
	v_mov_b32_e32 v128, v3
	v_mov_b32_e32 v129, v3
	s_waitcnt vmcnt(7) lgkmcnt(0)
	s_barrier
	ds_read_b128 v[42:45], v146
	ds_read_b128 v[38:41], v146 offset:2048
	ds_read_b128 v[10:13], v146 offset:4096
	ds_read_b128 v[6:9], v146 offset:6144
	ds_read_b128 v[22:25], v153 offset:32768
	ds_read_b128 v[18:21], v153 offset:34816
	ds_read_b128 v[30:33], v153 offset:36864
	ds_read_b128 v[26:29], v153 offset:38912
	ds_read_b128 v[34:37], v153 offset:40960
	ds_read_b128 v[14:17], v153 offset:43008
	v_lshl_or_b32 v2, v2, 15, v47
	v_lshl_or_b32 v2, v46, 11, v2
	v_lshl_add_u64 v[140:141], s[18:19], 0, v[2:3]
	v_lshl_add_u64 v[142:143], s[2:3], 0, v[2:3]
	s_mov_b32 s21, 0
	s_mov_b64 s[0:1], 0
	s_mov_b64 s[2:3], 0x100
	s_mov_b64 s[8:9], 0x20100
	s_mov_b64 s[16:17], 0x40100
	s_mov_b64 s[18:19], 0x60100
	v_mov_b32_e32 v2, v3
	v_mov_b32_e32 v4, v3
	v_mov_b32_e32 v5, v3
	v_mov_b32_e32 v46, v3
	v_mov_b32_e32 v47, v3
.LBB2_1:
	s_mul_i32 s22, s21, 0xe000
	v_add_u32_e32 v196, s22, v146
	v_add_u32_e32 v197, s22, v215
	s_add_u32 s46, s22, s45
	s_add_i32 s21, s21, 1
	s_waitcnt lgkmcnt(0)
	v_mfma_f32_16x16x32_f16 v[130:133], v[22:25], v[42:45], v[130:133]
	ds_read_b128 v[154:157], v196 offset:1024
	ds_read_b128 v[158:161], v196 offset:3072
	v_mfma_f32_16x16x32_f16 v[98:101], v[18:21], v[42:45], v[98:101]
	ds_read_b128 v[162:165], v196 offset:5120
	ds_read_b128 v[166:169], v196 offset:7168
	v_mfma_f32_16x16x32_f16 v[86:89], v[30:33], v[42:45], v[86:89]
	ds_read_b128 v[170:173], v197 offset:32768
	ds_read_b128 v[174:177], v197 offset:34816
	v_mfma_f32_16x16x32_f16 v[74:77], v[26:29], v[42:45], v[74:77]
	ds_read_b128 v[178:181], v197 offset:36864
	ds_read_b128 v[182:185], v197 offset:38912
	v_mfma_f32_16x16x32_f16 v[70:73], v[42:45], v[34:37], v[70:73]
	ds_read_b128 v[186:189], v197 offset:40960
	ds_read_b128 v[190:193], v197 offset:43008
	v_mfma_f32_16x16x32_f16 v[66:69], v[42:45], v[14:17], v[66:69]
	v_mfma_f32_16x16x32_f16 v[62:65], v[22:25], v[38:41], v[62:65]
	v_mfma_f32_16x16x32_f16 v[58:61], v[18:21], v[38:41], v[58:61]
	v_mfma_f32_16x16x32_f16 v[54:57], v[30:33], v[38:41], v[54:57]
	v_mfma_f32_16x16x32_f16 v[50:53], v[26:29], v[38:41], v[50:53]
	v_mfma_f32_16x16x32_f16 v[46:49], v[38:41], v[34:37], v[46:49]
	v_mfma_f32_16x16x32_f16 v[2:5], v[38:41], v[14:17], v[2:5]
	v_mfma_f32_16x16x32_f16 v[78:81], v[22:25], v[10:13], v[78:81]
	v_mfma_f32_16x16x32_f16 v[82:85], v[18:21], v[10:13], v[82:85]
	v_mfma_f32_16x16x32_f16 v[90:93], v[30:33], v[10:13], v[90:93]
	v_mfma_f32_16x16x32_f16 v[94:97], v[26:29], v[10:13], v[94:97]
	v_mfma_f32_16x16x32_f16 v[102:105], v[10:13], v[34:37], v[102:105]
	v_mfma_f32_16x16x32_f16 v[106:109], v[10:13], v[14:17], v[106:109]
	v_mfma_f32_16x16x32_f16 v[110:113], v[22:25], v[6:9], v[110:113]
	v_mfma_f32_16x16x32_f16 v[114:117], v[18:21], v[6:9], v[114:117]
	v_mfma_f32_16x16x32_f16 v[118:121], v[30:33], v[6:9], v[118:121]
	v_mfma_f32_16x16x32_f16 v[122:125], v[26:29], v[6:9], v[122:125]
	v_mfma_f32_16x16x32_f16 v[134:137], v[6:9], v[34:37], v[134:137]
	v_mfma_f32_16x16x32_f16 v[126:129], v[6:9], v[14:17], v[126:129]
	s_cmp_lg_u32 s21, 2
	s_cselect_b32 s21, s21, 0
	s_mul_i32 s22, s21, 0xe000
	v_add_u32_e32 v196, s22, v146
	v_add_u32_e32 v197, s22, v153
	s_waitcnt vmcnt(0) lgkmcnt(0)
	s_barrier
	s_mov_b32 m0, s46
	s_nop 0
	global_load_lds_dwordx4 v194, s[24:25]
	s_add_u32 m0, s46, 0x2000
	s_nop 0
	global_load_lds_dwordx4 v194, s[26:27]
	s_add_u32 m0, s46, 0x4000
	s_nop 0
	global_load_lds_dwordx4 v194, s[28:29]
	s_add_u32 m0, s46, 0x6000
	s_nop 0
	global_load_lds_dwordx4 v194, s[30:31]
	s_add_u32 m0, s46, 0x8000
	s_nop 0
	global_load_lds_dwordx4 v195, s[32:33]
	s_add_u32 m0, s46, 0xa000
	s_nop 0
	global_load_lds_dwordx4 v195, s[34:35]
	s_add_u32 m0, s46, 0xc000
	s_nop 0
	global_load_lds_dwordx4 v195, s[36:37]
	v_add_u32_e32 v194, 0x80, v194
	v_add_u32_e32 v195, 0x80, v195
	v_mfma_f32_16x16x32_f16 v[130:133], v[170:173], v[154:157], v[130:133]
	ds_read_b128 v[42:45], v196
	ds_read_b128 v[38:41], v196 offset:2048
	v_mfma_f32_16x16x32_f16 v[98:101], v[174:177], v[154:157], v[98:101]
	ds_read_b128 v[10:13], v196 offset:4096
	ds_read_b128 v[6:9], v196 offset:6144
	v_mfma_f32_16x16x32_f16 v[86:89], v[178:181], v[154:157], v[86:89]
	ds_read_b128 v[22:25], v197 offset:32768
	ds_read_b128 v[18:21], v197 offset:34816
	v_mfma_f32_16x16x32_f16 v[74:77], v[182:185], v[154:157], v[74:77]
	ds_read_b128 v[30:33], v197 offset:36864
	ds_read_b128 v[26:29], v197 offset:38912
	v_mfma_f32_16x16x32_f16 v[70:73], v[154:157], v[186:189], v[70:73]
	ds_read_b128 v[34:37], v197 offset:40960
	ds_read_b128 v[14:17], v197 offset:43008
	v_mfma_f32_16x16x32_f16 v[66:69], v[154:157], v[190:193], v[66:69]
	v_mfma_f32_16x16x32_f16 v[62:65], v[170:173], v[158:161], v[62:65]
	v_mfma_f32_16x16x32_f16 v[58:61], v[174:177], v[158:161], v[58:61]
	v_mfma_f32_16x16x32_f16 v[54:57], v[178:181], v[158:161], v[54:57]
	v_mfma_f32_16x16x32_f16 v[50:53], v[182:185], v[158:161], v[50:53]
	v_mfma_f32_16x16x32_f16 v[46:49], v[158:161], v[186:189], v[46:49]
	v_mfma_f32_16x16x32_f16 v[2:5], v[158:161], v[190:193], v[2:5]
	v_mfma_f32_16x16x32_f16 v[78:81], v[170:173], v[162:165], v[78:81]
	v_mfma_f32_16x16x32_f16 v[82:85], v[174:177], v[162:165], v[82:85]
	v_mfma_f32_16x16x32_f16 v[90:93], v[178:181], v[162:165], v[90:93]
	v_mfma_f32_16x16x32_f16 v[94:97], v[182:185], v[162:165], v[94:97]
	v_mfma_f32_16x16x32_f16 v[102:105], v[162:165], v[186:189], v[102:105]
	v_mfma_f32_16x16x32_f16 v[106:109], v[162:165], v[190:193], v[106:109]
	v_mfma_f32_16x16x32_f16 v[110:113], v[170:173], v[166:169], v[110:113]
	v_mfma_f32_16x16x32_f16 v[114:117], v[174:177], v[166:169], v[114:117]
	v_mfma_f32_16x16x32_f16 v[118:121], v[178:181], v[166:169], v[118:121]
	v_mfma_f32_16x16x32_f16 v[122:125], v[182:185], v[166:169], v[122:125]
	v_mfma_f32_16x16x32_f16 v[134:137], v[166:169], v[186:189], v[134:137]
	v_mfma_f32_16x16x32_f16 v[126:129], v[166:169], v[190:193], v[126:129]
	s_add_u32 s0, s0, 0x80
	s_addc_u32 s1, s1, 0
	s_cmpk_eq_i32 s0, 0x700
	s_cbranch_scc0 .LBB2_1
	s_waitcnt lgkmcnt(0)
	v_mfma_f32_16x16x32_f16 v[130:133], v[22:25], v[42:45], v[130:133]
	ds_read_b128 v[140:143], v146 offset:1024
	ds_read_b128 v[154:157], v146 offset:3072
	v_mfma_f32_16x16x32_f16 v[98:101], v[18:21], v[42:45], v[98:101]
	ds_read_b128 v[158:161], v146 offset:5120
	ds_read_b128 v[162:165], v146 offset:7168
	v_mfma_f32_16x16x32_f16 v[86:89], v[30:33], v[42:45], v[86:89]
	ds_read_b128 v[166:169], v215 offset:32768
	ds_read_b128 v[170:173], v215 offset:34816
	v_mfma_f32_16x16x32_f16 v[74:77], v[26:29], v[42:45], v[74:77]
	ds_read_b128 v[174:177], v215 offset:36864
	ds_read_b128 v[178:181], v215 offset:38912
	v_mfma_f32_16x16x32_f16 v[70:73], v[42:45], v[34:37], v[70:73]
	ds_read_b128 v[182:185], v215 offset:40960
	ds_read_b128 v[186:189], v215 offset:43008
	v_mfma_f32_16x16x32_f16 v[42:45], v[42:45], v[14:17], v[66:69]
	v_mfma_f32_16x16x32_f16 v[62:65], v[22:25], v[38:41], v[62:65]
	v_mfma_f32_16x16x32_f16 v[58:61], v[18:21], v[38:41], v[58:61]
	v_mfma_f32_16x16x32_f16 v[54:57], v[30:33], v[38:41], v[54:57]
	v_mfma_f32_16x16x32_f16 v[50:53], v[26:29], v[38:41], v[50:53]
	v_mfma_f32_16x16x32_f16 v[46:49], v[38:41], v[34:37], v[46:49]
	v_mfma_f32_16x16x32_f16 v[2:5], v[38:41], v[14:17], v[2:5]
	v_mfma_f32_16x16x32_f16 v[38:41], v[22:25], v[10:13], v[78:81]
	v_mfma_f32_16x16x32_f16 v[66:69], v[18:21], v[10:13], v[82:85]
	v_mfma_f32_16x16x32_f16 v[78:81], v[30:33], v[10:13], v[90:93]
	v_mfma_f32_16x16x32_f16 v[82:85], v[26:29], v[10:13], v[94:97]
	v_mfma_f32_16x16x32_f16 v[90:93], v[10:13], v[34:37], v[102:105]
	v_mfma_f32_16x16x32_f16 v[94:97], v[10:13], v[14:17], v[106:109]
	v_mfma_f32_16x16x32_f16 v[22:25], v[22:25], v[6:9], v[110:113]
	v_mfma_f32_16x16x32_f16 v[102:105], v[18:21], v[6:9], v[114:117]
	v_or_b32_e32 v21, v151, v152
	v_and_b32_e32 v20, 63, v0
	v_mfma_f32_16x16x32_f16 v[30:33], v[30:33], v[6:9], v[118:121]
	v_mfma_f32_16x16x32_f16 v[26:29], v[26:29], v[6:9], v[122:125]
	v_mfma_f32_16x16x32_f16 v[34:37], v[6:9], v[34:37], v[134:137]
	v_mfma_f32_16x16x32_f16 v[6:9], v[6:9], v[14:17], v[126:129]
	v_add_u32_e32 v10, 0x16800, v21
	s_waitcnt vmcnt(0) lgkmcnt(0)
	s_waitcnt lgkmcnt(0)
	v_mfma_f32_16x16x32_f16 v[16:19], v[166:169], v[140:143], v[130:133]
	s_barrier
	ds_read_b128 v[106:109], v146 offset:57344
	ds_read_b128 v[110:113], v146 offset:59392
	v_mfma_f32_16x16x32_f16 v[98:101], v[170:173], v[140:143], v[98:101]
	ds_read_b128 v[114:117], v146 offset:61440
	ds_read_b128 v[12:15], v146 offset:63488
	v_add_u32_e32 v0, 0x16000, v21
	v_mfma_f32_16x16x32_f16 v[86:89], v[174:177], v[140:143], v[86:89]
	ds_read_b128 v[122:125], v10
	v_add_u32_e32 v10, 0x17000, v21
	ds_read_b128 v[118:121], v0
	v_mfma_f32_16x16x32_f16 v[74:77], v[178:181], v[140:143], v[74:77]
	ds_read_b128 v[126:129], v10
	v_add_u32_e32 v10, 0x17800, v21
	ds_read_b128 v[130:133], v10
	v_mfma_f32_16x16x32_f16 v[70:73], v[140:143], v[182:185], v[70:73]
	ds_read_b128 v[134:137], v0 offset:8192
	ds_read_b128 v[190:193], v0 offset:10240
	v_mfma_f32_16x16x32_f16 v[42:45], v[140:143], v[186:189], v[42:45]
	v_mfma_f32_16x16x32_f16 v[62:65], v[166:169], v[154:157], v[62:65]
	v_mfma_f32_16x16x32_f16 v[58:61], v[170:173], v[154:157], v[58:61]
	v_mfma_f32_16x16x32_f16 v[54:57], v[174:177], v[154:157], v[54:57]
	v_mfma_f32_16x16x32_f16 v[50:53], v[178:181], v[154:157], v[50:53]
	v_mfma_f32_16x16x32_f16 v[46:49], v[154:157], v[182:185], v[46:49]
	v_mfma_f32_16x16x32_f16 v[140:143], v[154:157], v[186:189], v[2:5]
	v_mfma_f32_16x16x32_f16 v[38:41], v[166:169], v[158:161], v[38:41]
	v_mfma_f32_16x16x32_f16 v[66:69], v[170:173], v[158:161], v[66:69]
	v_mfma_f32_16x16x32_f16 v[78:81], v[174:177], v[158:161], v[78:81]
	v_mfma_f32_16x16x32_f16 v[82:85], v[178:181], v[158:161], v[82:85]
	v_mfma_f32_16x16x32_f16 v[90:93], v[158:161], v[182:185], v[90:93]
	v_mfma_f32_16x16x32_f16 v[94:97], v[158:161], v[186:189], v[94:97]
	v_mfma_f32_16x16x32_f16 v[22:25], v[166:169], v[162:165], v[22:25]
	v_mfma_f32_16x16x32_f16 v[102:105], v[170:173], v[162:165], v[102:105]
	v_mfma_f32_16x16x32_f16 v[30:33], v[174:177], v[162:165], v[30:33]
	v_mfma_f32_16x16x32_f16 v[26:29], v[178:181], v[162:165], v[26:29]
	v_mfma_f32_16x16x32_f16 v[34:37], v[162:165], v[182:185], v[34:37]
	v_mfma_f32_16x16x32_f16 v[152:155], v[162:165], v[186:189], v[6:9]
	s_waitcnt lgkmcnt(0)
	v_mfma_f32_16x16x32_f16 v[156:159], v[118:121], v[106:109], v[16:19]
	s_movk_i32 s0, 0x7c0
	v_add_u32_e32 v216, 0x16000, v215
	ds_read_b128 v[202:205], v216 offset:8192
	ds_read_b128 v[206:209], v216 offset:10240
	v_lshlrev_b32_e32 v16, 6, v144
	v_mov_b32_e32 v17, 0
	v_mov_b32_e32 v139, v17
	v_lshl_add_u64 v[4:5], s[6:7], 0, v[16:17]
	v_lshl_add_u64 v[8:9], v[4:5], 0, v[138:139]
	s_waitcnt vmcnt(0)
	v_lshlrev_b32_e32 v4, 5, v150
	v_lshl_add_u64 v[2:3], s[4:5], 0, v[16:17]
	v_ashrrev_i32_e32 v5, 31, v4
	v_lshl_add_u64 v[2:3], v[2:3], 0, v[138:139]
	v_lshlrev_b64 v[4:5], 2, v[4:5]
	v_lshl_add_u64 v[6:7], v[2:3], 0, v[4:5]
	v_lshl_add_u64 v[4:5], v[8:9], 0, v[4:5]
	v_mfma_f32_16x16x32_f16 v[98:101], v[122:125], v[106:109], v[98:101]
	global_load_dwordx4 v[160:163], v[6:7], off
	v_lshlrev_b32_e32 v18, 5, v147
	v_ashrrev_i32_e32 v19, 31, v18
	v_mfma_f32_16x16x32_f16 v[86:89], v[126:129], v[106:109], v[86:89]
	v_lshlrev_b64 v[18:19], 2, v[18:19]
	ds_read_b128 v[172:175], v146 offset:62464
	ds_read_b128 v[176:179], v146 offset:64512
	v_mfma_f32_16x16x32_f16 v[74:77], v[130:133], v[106:109], v[74:77]
	v_mfma_f32_16x16x32_f16 v[70:73], v[106:109], v[134:137], v[70:73]
	v_mfma_f32_16x16x32_f16 v[42:45], v[106:109], v[190:193], v[42:45]
	global_load_dwordx4 v[106:109], v[4:5], off
	v_lshlrev_b32_e32 v4, 5, v149
	v_ashrrev_i32_e32 v5, 31, v4
	v_lshlrev_b64 v[4:5], 2, v[4:5]
	v_lshl_add_u64 v[6:7], v[2:3], 0, v[4:5]
	v_lshl_add_u64 v[4:5], v[8:9], 0, v[4:5]
	global_load_dwordx4 v[168:171], v[4:5], off
	global_load_dwordx4 v[164:167], v[6:7], off
	v_lshlrev_b32_e32 v4, 5, v148
	v_ashrrev_i32_e32 v5, 31, v4
	v_lshlrev_b64 v[10:11], 2, v[4:5]
	v_lshl_add_u64 v[4:5], v[2:3], 0, v[10:11]
	v_lshl_add_u64 v[10:11], v[8:9], 0, v[10:11]
	global_load_dwordx4 v[210:213], v[10:11], off
	v_lshl_add_u64 v[2:3], v[2:3], 0, v[18:19]
	global_load_dwordx4 v[4:7], v[4:5], off
	v_lshl_add_u64 v[8:9], v[8:9], 0, v[18:19]
	v_add_u32_e32 v18, 0x16000, v215
	v_ashrrev_i32_e32 v10, 7, v145
	ds_read_b128 v[180:183], v18
	v_add_u32_e32 v18, 0x17000, v215
	v_and_b32_e32 v10, -16, v10
	v_add_u32_e32 v19, 0x16800, v215
	ds_read_b128 v[194:197], v18
	v_add_u32_e32 v18, s20, v10
	global_load_dwordx4 v[8:11], v[8:9], off
	ds_read_b128 v[184:187], v19
	v_add_u32_e32 v19, 0x17800, v215
	v_and_or_b32 v21, v145, s0, v1
	global_load_dwordx4 v[0:3], v[2:3], off
	v_mfma_f32_16x16x32_f16 v[62:65], v[118:121], v[110:113], v[62:65]
	ds_read_b128 v[198:201], v19
	v_ashrrev_i32_e32 v19, 31, v18
	ds_read_b128 v[148:151], v146 offset:60416
	v_mfma_f32_16x16x32_f16 v[58:61], v[122:125], v[110:113], v[58:61]
	v_mfma_f32_16x16x32_f16 v[54:57], v[126:129], v[110:113], v[54:57]
	v_mfma_f32_16x16x32_f16 v[50:53], v[130:133], v[110:113], v[50:53]
	v_mfma_f32_16x16x32_f16 v[46:49], v[110:113], v[134:137], v[46:49]
	v_mfma_f32_16x16x32_f16 v[110:113], v[110:113], v[190:193], v[140:143]
	s_nop 2
	ds_read_b128 v[140:143], v146 offset:58368
	v_mfma_f32_16x16x32_f16 v[38:41], v[118:121], v[114:117], v[38:41]
	v_mfma_f32_16x16x32_f16 v[66:69], v[122:125], v[114:117], v[66:69]
	v_mfma_f32_16x16x32_f16 v[78:81], v[126:129], v[114:117], v[78:81]
	v_mfma_f32_16x16x32_f16 v[82:85], v[130:133], v[114:117], v[82:85]
	v_mfma_f32_16x16x32_f16 v[90:93], v[114:117], v[134:137], v[90:93]
	v_mfma_f32_16x16x32_f16 v[94:97], v[114:117], v[190:193], v[94:97]
	s_waitcnt lgkmcnt(0)
	v_mfma_f32_16x16x32_f16 v[114:117], v[180:183], v[140:143], v[156:159]
	v_mfma_f32_16x16x32_f16 v[98:101], v[184:187], v[140:143], v[98:101]
	v_mfma_f32_16x16x32_f16 v[22:25], v[118:121], v[12:15], v[22:25]
	s_waitcnt vmcnt(6)
	s_nop 4
	v_pk_mul_f32 v[120:121], v[114:115], v[106:107] op_sel_hi:[1,0]
	v_lshlrev_b64 v[118:119], 17, v[18:19]
	v_lshl_or_b32 v118, v21, 6, v118
	v_mfma_f32_16x16x32_f16 v[102:105], v[122:125], v[12:15], v[102:105]
	v_mul_f32_e64 v122, v116, v107
	v_mul_f32_e64 v123, v117, v107
	v_pk_fma_f32 v[124:125], v[114:115], v[160:161], v[120:121] op_sel:[0,0,1] op_sel_hi:[1,1,0] neg_lo:[0,0,1] neg_hi:[0,0,1]
	v_pk_fma_f32 v[114:115], v[114:115], v[160:161], v[120:121] op_sel:[0,0,1] op_sel_hi:[1,0,0]
	v_pk_fma_f32 v[120:121], v[116:117], v[160:161], v[122:123] op_sel:[0,1,1] op_sel_hi:[1,1,0] neg_lo:[0,0,1] neg_hi:[0,0,1]
	v_pk_fma_f32 v[116:117], v[116:117], v[160:161], v[122:123] op_sel:[0,1,1] op_sel_hi:[1,1,0]
	v_cvt_pk_f16_f32 v114, v124, v115
	v_cvt_pk_f16_f32 v115, v120, v117
	v_pk_mul_f32 v[116:117], v[98:99], v[108:109] op_sel_hi:[1,0]
	v_mov_b32_e32 v122, v163
	v_pk_fma_f32 v[120:121], v[98:99], v[162:163], v[116:117] op_sel:[0,0,1] op_sel_hi:[1,1,0] neg_lo:[0,0,1] neg_hi:[0,0,1]
	v_pk_fma_f32 v[98:99], v[98:99], v[162:163], v[116:117] op_sel:[0,0,1] op_sel_hi:[1,0,0]
	v_mfma_f32_16x16x32_f16 v[30:33], v[126:129], v[12:15], v[30:33]
	v_cvt_pk_f16_f32 v116, v120, v99
	v_mov_b32_e32 v120, v109
	v_pk_mul_f32 v[98:99], v[100:101], v[120:121] op_sel_hi:[1,0]
	v_mfma_f32_16x16x32_f16 v[26:29], v[130:133], v[12:15], v[26:29]
	v_fma_f32 v124, v100, v122, -v99
	v_fma_f32 v125, v101, v122, -v98
	v_pk_fma_f32 v[98:99], v[100:101], v[122:123], v[98:99] op_sel:[0,0,1] op_sel_hi:[1,0,0]
	s_nop 0
	v_cvt_pk_f16_f32 v117, v124, v99
	v_lshlrev_b64 v[124:125], 1, v[118:119]
	v_lshl_add_u64 v[126:127], s[10:11], 0, v[124:125]
	v_mfma_f32_16x16x32_f16 v[34:37], v[12:15], v[134:137], v[34:37]
	v_mfma_f32_16x16x32_f16 v[98:101], v[12:15], v[190:193], v[152:155]
	v_lshl_add_u64 v[12:13], v[126:127], 0, v[16:17]
	v_lshl_add_u64 v[126:127], v[12:13], 0, v[138:139]
	global_store_dwordx4 v[126:127], v[114:117], off sc1
	v_mfma_f32_16x16x32_f16 v[12:15], v[194:197], v[140:143], v[86:89]
	v_mfma_f32_16x16x32_f16 v[74:77], v[198:201], v[140:143], v[74:77]
	v_mfma_f32_16x16x32_f16 v[58:61], v[184:187], v[148:151], v[58:61]
	s_nop 5
	v_mul_f32_e64 v86, v12, v106
	v_mul_f32_e64 v87, v13, v106
	v_pk_fma_f32 v[88:89], v[12:13], v[160:161], v[86:87] op_sel:[0,0,1] op_sel_hi:[1,1,0] neg_lo:[0,0,1] neg_hi:[0,0,1]
	v_pk_fma_f32 v[12:13], v[12:13], v[160:161], v[86:87] op_sel:[0,0,1] op_sel_hi:[1,0,0]
	v_mfma_f32_16x16x32_f16 v[54:57], v[194:197], v[148:151], v[54:57]
	v_cvt_pk_f16_f32 v86, v88, v13
	v_pk_mul_f32 v[12:13], v[14:15], v[106:107] op_sel:[0,1]
	s_nop 0
	v_pk_fma_f32 v[88:89], v[14:15], v[160:161], v[12:13] op_sel:[0,1,1] op_sel_hi:[1,1,0] neg_lo:[0,0,1] neg_hi:[0,0,1]
	v_pk_fma_f32 v[12:13], v[14:15], v[160:161], v[12:13] op_sel:[0,1,1] op_sel_hi:[1,1,0]
	v_mfma_f32_16x16x32_f16 v[50:53], v[198:201], v[148:151], v[50:53]
	v_cvt_pk_f16_f32 v87, v88, v13
	v_pk_mul_f32 v[88:89], v[74:75], v[108:109] op_sel_hi:[1,0]
	v_mfma_f32_16x16x32_f16 v[12:15], v[140:143], v[206:209], v[42:45]
	s_nop 2
	v_fma_f32 v42, v74, v162, -v89
	v_fma_f32 v43, v75, v163, -v88
	v_pk_fma_f32 v[44:45], v[74:75], v[162:163], v[88:89] op_sel:[0,0,1] op_sel_hi:[1,0,0]
	v_mfma_f32_16x16x32_f16 v[38:41], v[180:183], v[172:175], v[38:41]
	v_cvt_pk_f16_f32 v88, v42, v45
	v_mfma_f32_16x16x32_f16 v[42:45], v[180:183], v[148:151], v[62:65]
	s_nop 2
	v_mul_f32_e64 v62, v76, v120
	v_mul_f32_e64 v63, v77, v120
	v_mfma_f32_16x16x32_f16 v[66:69], v[184:187], v[172:175], v[66:69]
	v_fma_f32 v64, v76, v122, -v63
	v_fma_f32 v65, v77, v122, -v62
	v_pk_fma_f32 v[62:63], v[76:77], v[122:123], v[62:63] op_sel:[0,0,1] op_sel_hi:[1,0,0]
	s_nop 0
	v_cvt_pk_f16_f32 v89, v64, v63
	v_lshl_add_u64 v[62:63], s[12:13], 0, v[124:125]
	v_lshl_add_u64 v[62:63], v[62:63], 0, v[16:17]
	v_lshl_add_u64 v[106:107], v[62:63], 0, v[138:139]
	s_waitcnt vmcnt(6)
	v_pk_mul_f32 v[62:63], v[42:43], v[168:169] op_sel_hi:[1,0]
	global_store_dwordx4 v[106:107], v[86:89], off sc1
	s_waitcnt vmcnt(6)
	v_pk_fma_f32 v[64:65], v[42:43], v[164:165], v[62:63] op_sel:[0,0,1] op_sel_hi:[1,1,0] neg_lo:[0,0,1] neg_hi:[0,0,1]
	v_pk_fma_f32 v[42:43], v[42:43], v[164:165], v[62:63] op_sel:[0,0,1] op_sel_hi:[1,0,0]
	v_pk_mul_f32 v[62:63], v[44:45], v[168:169] op_sel:[0,1]
	v_cvt_pk_f16_f32 v42, v64, v43
	v_pk_fma_f32 v[74:75], v[44:45], v[164:165], v[62:63] op_sel:[0,1,1] op_sel_hi:[1,1,0] neg_lo:[0,0,1] neg_hi:[0,0,1]
	v_pk_fma_f32 v[44:45], v[44:45], v[164:165], v[62:63] op_sel:[0,1,1] op_sel_hi:[1,1,0]
	v_mov_b32_e32 v86, v171
	v_cvt_pk_f16_f32 v43, v74, v45
	v_pk_mul_f32 v[44:45], v[58:59], v[170:171] op_sel_hi:[1,0]
	v_mov_b32_e32 v88, v167
	v_pk_fma_f32 v[74:75], v[58:59], v[166:167], v[44:45] op_sel:[0,0,1] op_sel_hi:[1,1,0] neg_lo:[0,0,1] neg_hi:[0,0,1]
	v_pk_fma_f32 v[44:45], v[58:59], v[166:167], v[44:45] op_sel:[0,0,1] op_sel_hi:[1,0,0]
	v_pk_mul_f32 v[58:59], v[60:61], v[86:87] op_sel_hi:[1,0]
	v_cvt_pk_f16_f32 v44, v74, v45
	v_pk_fma_f32 v[108:109], v[60:61], v[88:89], v[58:59] op_sel:[0,0,1] op_sel_hi:[1,0,0] neg_lo:[0,0,1] neg_hi:[0,0,1]
	v_pk_fma_f32 v[58:59], v[60:61], v[88:89], v[58:59] op_sel:[0,0,1] op_sel_hi:[1,0,0]
	v_mfma_f32_16x16x32_f16 v[74:77], v[194:197], v[172:175], v[78:81]
	v_cvt_pk_f16_f32 v45, v108, v59
	global_store_dwordx4 v[126:127], v[42:45], off offset:2048 sc1
	v_pk_mul_f32 v[58:59], v[54:55], v[168:169] op_sel_hi:[1,0]
	v_mfma_f32_16x16x32_f16 v[22:25], v[180:183], v[176:179], v[22:25]
	v_fma_f32 v78, v54, v164, -v59
	v_fma_f32 v79, v55, v165, -v58
	v_pk_fma_f32 v[54:55], v[54:55], v[164:165], v[58:59] op_sel:[0,0,1] op_sel_hi:[1,0,0]
	v_mfma_f32_16x16x32_f16 v[42:45], v[198:201], v[172:175], v[82:85]
	v_cvt_pk_f16_f32 v54, v78, v55
	s_nop 1
	v_pk_mul_f32 v[82:83], v[56:57], v[168:169] op_sel:[0,1]
	v_mfma_f32_16x16x32_f16 v[30:33], v[194:197], v[176:179], v[30:33]
	v_fma_f32 v84, v56, v165, -v83
	v_fma_f32 v85, v57, v165, -v82
	v_pk_fma_f32 v[56:57], v[56:57], v[164:165], v[82:83] op_sel:[0,1,1] op_sel_hi:[1,1,0]
	s_nop 0
	v_cvt_pk_f16_f32 v55, v84, v57
	v_pk_mul_f32 v[56:57], v[50:51], v[170:171] op_sel_hi:[1,0]
	v_mfma_f32_16x16x32_f16 v[26:29], v[198:201], v[176:179], v[26:29]
	v_fma_f32 v82, v50, v166, -v57
	v_fma_f32 v83, v51, v167, -v56
	v_pk_fma_f32 v[50:51], v[50:51], v[166:167], v[56:57] op_sel:[0,0,1] op_sel_hi:[1,0,0]
	s_nop 0
	v_cvt_pk_f16_f32 v56, v82, v51
	v_pk_mul_f32 v[50:51], v[52:53], v[86:87] op_sel_hi:[1,0]
	v_mfma_f32_16x16x32_f16 v[82:85], v[184:187], v[176:179], v[102:105]
	v_fma_f32 v86, v52, v88, -v51
	v_fma_f32 v87, v53, v88, -v50
	v_pk_fma_f32 v[50:51], v[52:53], v[88:89], v[50:51] op_sel:[0,0,1] op_sel_hi:[1,0,0]
	s_nop 0
	v_cvt_pk_f16_f32 v57, v86, v51
	global_store_dwordx4 v[106:107], v[54:57], off offset:2048 sc1
	s_waitcnt vmcnt(7)
	v_pk_mul_f32 v[50:51], v[38:39], v[210:211] op_sel_hi:[1,0]
	v_mfma_f32_16x16x32_f16 v[70:73], v[140:143], v[202:205], v[70:73]
	v_mul_f32_e64 v56, v40, v211
	v_mul_f32_e64 v57, v41, v211
	s_waitcnt vmcnt(6)
	v_pk_fma_f32 v[52:53], v[38:39], v[4:5], v[50:51] op_sel:[0,0,1] op_sel_hi:[1,1,0] neg_lo:[0,0,1] neg_hi:[0,0,1]
	v_pk_fma_f32 v[38:39], v[38:39], v[4:5], v[50:51] op_sel:[0,0,1] op_sel_hi:[1,0,0]
	v_pk_fma_f32 v[86:87], v[40:41], v[4:5], v[56:57] op_sel:[0,1,1] op_sel_hi:[1,1,0] neg_lo:[0,0,1] neg_hi:[0,0,1]
	v_pk_fma_f32 v[40:41], v[40:41], v[4:5], v[56:57] op_sel:[0,1,1] op_sel_hi:[1,1,0]
	v_cvt_pk_f16_f32 v38, v52, v39
	v_cvt_pk_f16_f32 v39, v86, v41
	v_pk_mul_f32 v[40:41], v[66:67], v[212:213] op_sel_hi:[1,0]
	v_or_b32_e32 v54, 0x800, v118
	v_pk_fma_f32 v[56:57], v[66:67], v[6:7], v[40:41] op_sel:[0,0,1] op_sel_hi:[1,1,0] neg_lo:[0,0,1] neg_hi:[0,0,1]
	v_pk_fma_f32 v[40:41], v[66:67], v[6:7], v[40:41] op_sel:[0,0,1] op_sel_hi:[1,0,0]
	v_mov_b32_e32 v55, v119
	v_cvt_pk_f16_f32 v40, v56, v41
	v_mov_b32_e32 v56, v213
	v_pk_mul_f32 v[66:67], v[68:69], v[56:57] op_sel_hi:[1,0]
	v_mov_b32_e32 v86, v7
	v_pk_fma_f32 v[88:89], v[68:69], v[86:87], v[66:67] op_sel:[0,0,1] op_sel_hi:[1,0,0] neg_lo:[0,0,1] neg_hi:[0,0,1]
	v_pk_fma_f32 v[66:67], v[68:69], v[86:87], v[66:67] op_sel:[0,0,1] op_sel_hi:[1,0,0]
	v_lshlrev_b64 v[54:55], 1, v[54:55]
	v_cvt_pk_f16_f32 v41, v88, v67
	v_lshl_add_u64 v[66:67], s[10:11], 0, v[54:55]
	v_lshl_add_u64 v[66:67], v[66:67], 0, v[16:17]
	v_lshl_add_u64 v[66:67], v[66:67], 0, v[138:139]
	global_store_dwordx4 v[66:67], v[38:41], off sc1
	v_or_b32_e32 v118, 0xc00, v118
	v_mfma_f32_16x16x32_f16 v[46:49], v[148:151], v[202:205], v[46:49]
	v_mul_f32_e64 v38, v74, v210
	v_mul_f32_e64 v39, v75, v210
	v_pk_fma_f32 v[40:41], v[74:75], v[4:5], v[38:39] op_sel:[0,0,1] op_sel_hi:[1,1,0] neg_lo:[0,0,1] neg_hi:[0,0,1]
	v_pk_fma_f32 v[38:39], v[74:75], v[4:5], v[38:39] op_sel:[0,0,1] op_sel_hi:[1,0,0]
	v_mfma_f32_16x16x32_f16 v[58:61], v[172:175], v[202:205], v[90:93]
	v_cvt_pk_f16_f32 v38, v40, v39
	v_pk_mul_f32 v[40:41], v[76:77], v[210:211] op_sel:[0,1]
	s_nop 0
	v_pk_fma_f32 v[66:67], v[76:77], v[4:5], v[40:41] op_sel:[0,1,1] op_sel_hi:[1,1,0] neg_lo:[0,0,1] neg_hi:[0,0,1]
	v_pk_fma_f32 v[4:5], v[76:77], v[4:5], v[40:41] op_sel:[0,1,1] op_sel_hi:[1,1,0]
	v_mfma_f32_16x16x32_f16 v[34:37], v[176:179], v[202:205], v[34:37]
	v_cvt_pk_f16_f32 v39, v66, v5
	v_pk_mul_f32 v[4:5], v[42:43], v[212:213] op_sel_hi:[1,0]
	s_nop 0
	v_pk_fma_f32 v[40:41], v[42:43], v[6:7], v[4:5] op_sel:[0,0,1] op_sel_hi:[1,1,0] neg_lo:[0,0,1] neg_hi:[0,0,1]
	v_pk_fma_f32 v[4:5], v[42:43], v[6:7], v[4:5] op_sel:[0,0,1] op_sel_hi:[1,0,0]
	v_mfma_f32_16x16x32_f16 v[62:65], v[148:151], v[206:209], v[110:113]
	v_cvt_pk_f16_f32 v40, v40, v5
	v_pk_mul_f32 v[4:5], v[44:45], v[56:57] op_sel_hi:[1,0]
	s_nop 0
	v_pk_fma_f32 v[6:7], v[44:45], v[86:87], v[4:5] op_sel:[0,0,1] op_sel_hi:[1,0,0] neg_lo:[0,0,1] neg_hi:[0,0,1]
	v_pk_fma_f32 v[4:5], v[44:45], v[86:87], v[4:5] op_sel:[0,0,1] op_sel_hi:[1,0,0]
	v_mfma_f32_16x16x32_f16 v[78:81], v[172:175], v[206:209], v[94:97]
	v_cvt_pk_f16_f32 v41, v6, v5
	v_lshl_add_u64 v[4:5], s[12:13], 0, v[54:55]
	v_lshl_add_u64 v[4:5], v[4:5], 0, v[16:17]
	v_lshl_add_u64 v[4:5], v[4:5], 0, v[138:139]
	global_store_dwordx4 v[4:5], v[38:41], off sc1
	s_waitcnt vmcnt(7)
	v_pk_mul_f32 v[4:5], v[22:23], v[8:9] op_sel_hi:[1,0]
	v_mfma_f32_16x16x32_f16 v[50:53], v[176:179], v[206:209], v[98:101]
	s_waitcnt vmcnt(6)
	v_pk_fma_f32 v[6:7], v[22:23], v[0:1], v[4:5] op_sel:[0,0,1] op_sel_hi:[1,1,0] neg_lo:[0,0,1] neg_hi:[0,0,1]
	v_pk_fma_f32 v[4:5], v[22:23], v[0:1], v[4:5] op_sel:[0,0,1] op_sel_hi:[1,0,0]
	v_mov_b32_e32 v38, v3
	v_cvt_pk_f16_f32 v4, v6, v5
	v_pk_mul_f32 v[6:7], v[24:25], v[8:9] op_sel:[0,1]
	s_nop 0
	v_pk_fma_f32 v[22:23], v[24:25], v[0:1], v[6:7] op_sel:[0,1,1] op_sel_hi:[1,1,0] neg_lo:[0,0,1] neg_hi:[0,0,1]
	v_pk_fma_f32 v[6:7], v[24:25], v[0:1], v[6:7] op_sel:[0,1,1] op_sel_hi:[1,1,0]
	s_nop 0
	v_cvt_pk_f16_f32 v5, v22, v7
	v_pk_mul_f32 v[6:7], v[82:83], v[10:11] op_sel_hi:[1,0]
	s_nop 0
	v_pk_fma_f32 v[22:23], v[82:83], v[2:3], v[6:7] op_sel:[0,0,1] op_sel_hi:[1,1,0] neg_lo:[0,0,1] neg_hi:[0,0,1]
	v_pk_fma_f32 v[6:7], v[82:83], v[2:3], v[6:7] op_sel:[0,0,1] op_sel_hi:[1,0,0]
	s_nop 0
	v_cvt_pk_f16_f32 v6, v22, v7
	v_mov_b32_e32 v22, v11
	v_pk_mul_f32 v[24:25], v[84:85], v[22:23] op_sel_hi:[1,0]
	s_nop 0
	v_pk_fma_f32 v[40:41], v[84:85], v[38:39], v[24:25] op_sel:[0,0,1] op_sel_hi:[1,0,0] neg_lo:[0,0,1] neg_hi:[0,0,1]
	v_pk_fma_f32 v[24:25], v[84:85], v[38:39], v[24:25] op_sel:[0,0,1] op_sel_hi:[1,0,0]
	s_nop 0
	v_cvt_pk_f16_f32 v7, v40, v25
	v_lshlrev_b64 v[24:25], 1, v[118:119]
	v_lshl_add_u64 v[40:41], s[10:11], 0, v[24:25]
	v_lshl_add_u64 v[40:41], v[40:41], 0, v[16:17]
	v_lshl_add_u64 v[40:41], v[40:41], 0, v[138:139]
	global_store_dwordx4 v[40:41], v[4:7], off sc1
	s_nop 1
	v_pk_mul_f32 v[4:5], v[30:31], v[8:9] op_sel_hi:[1,0]
	s_nop 0
	v_pk_fma_f32 v[6:7], v[30:31], v[0:1], v[4:5] op_sel:[0,0,1] op_sel_hi:[1,1,0] neg_lo:[0,0,1] neg_hi:[0,0,1]
	v_pk_fma_f32 v[4:5], v[30:31], v[0:1], v[4:5] op_sel:[0,0,1] op_sel_hi:[1,0,0]
	s_nop 0
	v_cvt_pk_f16_f32 v4, v6, v5
	v_pk_mul_f32 v[6:7], v[32:33], v[8:9] op_sel:[0,1]
	s_nop 0
	v_pk_fma_f32 v[8:9], v[32:33], v[0:1], v[6:7] op_sel:[0,1,1] op_sel_hi:[1,1,0] neg_lo:[0,0,1] neg_hi:[0,0,1]
	v_pk_fma_f32 v[0:1], v[32:33], v[0:1], v[6:7] op_sel:[0,1,1] op_sel_hi:[1,1,0]
	s_nop 0
	v_cvt_pk_f16_f32 v5, v8, v1
	v_pk_mul_f32 v[0:1], v[26:27], v[10:11] op_sel_hi:[1,0]
	s_nop 0
	v_pk_fma_f32 v[6:7], v[26:27], v[2:3], v[0:1] op_sel:[0,0,1] op_sel_hi:[1,1,0] neg_lo:[0,0,1] neg_hi:[0,0,1]
	v_pk_fma_f32 v[0:1], v[26:27], v[2:3], v[0:1] op_sel:[0,0,1] op_sel_hi:[1,0,0]
	s_nop 0
	v_cvt_pk_f16_f32 v6, v6, v1
	v_pk_mul_f32 v[0:1], v[28:29], v[22:23] op_sel_hi:[1,0]
	s_nop 0
	v_pk_fma_f32 v[2:3], v[28:29], v[38:39], v[0:1] op_sel:[0,0,1] op_sel_hi:[1,0,0] neg_lo:[0,0,1] neg_hi:[0,0,1]
	v_pk_fma_f32 v[0:1], v[28:29], v[38:39], v[0:1] op_sel:[0,0,1] op_sel_hi:[1,0,0]
	v_cvt_pk_f16_f32 v3, v48, v49
	v_cvt_pk_f16_f32 v7, v2, v1
	v_lshl_add_u64 v[0:1], s[12:13], 0, v[24:25]
	v_lshl_add_u64 v[0:1], v[0:1], 0, v[16:17]
	v_lshl_add_u64 v[0:1], v[0:1], 0, v[138:139]
	global_store_dwordx4 v[0:1], v[4:7], off sc1
	v_lshlrev_b64 v[0:1], 18, v[18:19]
	v_lshlrev_b32_e32 v2, 7, v145
	v_lshl_add_u64 v[0:1], s[14:15], 0, v[0:1]
	v_and_b32_e32 v16, 0x3e000, v2
	v_lshl_add_u64 v[0:1], v[0:1], 0, v[16:17]
	v_lshlrev_b32_e32 v16, 4, v20
	v_lshl_add_u64 v[4:5], v[0:1], 0, v[16:17]
	v_lshlrev_b32_e32 v16, 12, v144
	v_cvt_pk_f16_f32 v2, v46, v47
	v_cvt_pk_f16_f32 v1, v72, v73
	v_cvt_pk_f16_f32 v0, v70, v71
	v_lshl_add_u64 v[4:5], v[4:5], 0, v[16:17]
	global_store_dwordx4 v[4:5], v[0:3], off sc1
	s_nop 1
	v_cvt_pk_f16_f32 v3, v36, v37
	v_cvt_pk_f16_f32 v2, v34, v35
	v_cvt_pk_f16_f32 v1, v60, v61
	v_cvt_pk_f16_f32 v0, v58, v59
	global_store_dwordx4 v[4:5], v[0:3], off offset:1024 sc1
	s_nop 1
	v_cvt_pk_f16_f32 v3, v64, v65
	v_cvt_pk_f16_f32 v2, v62, v63
	v_cvt_pk_f16_f32 v1, v14, v15
	v_cvt_pk_f16_f32 v0, v12, v13
	global_store_dwordx4 v[4:5], v[0:3], off offset:2048 sc1
	s_nop 1
	v_cvt_pk_f16_f32 v3, v52, v53
	v_cvt_pk_f16_f32 v2, v50, v51
	v_cvt_pk_f16_f32 v1, v80, v81
	v_cvt_pk_f16_f32 v0, v78, v79
	global_store_dwordx4 v[4:5], v[0:3], off offset:3072 sc1
	s_endpgm
	.p2align	8
